# grid barrier: acquire invalidate issued at arrival, last XCD leader bumps all per-XCD generation words
# speedup vs baseline: 1.0300x; 1.0216x over previous
.LBB0_70:
	v_readlane_b32 s2, v253, 36
	s_lshl_b32 s2, s2, 8
	v_readlane_b32 s4, v253, 34
	v_readlane_b32 s5, v253, 35
	s_add_u32 s2, s4, s2
	s_addc_u32 s3, s5, 0
	v_mov_b32_e32 v2, 0x1000
	v_mov_b32_e32 v4, 1
	global_atomic_add v4, v2, v4, s[2:3] offset:1024 sc0
	v_cvt_f32_u32_e32 v2, v3
	v_sub_u32_e32 v5, 0, v3
	v_rcp_iflag_f32_e32 v2, v2
	s_nop 0
	v_mul_f32_e32 v2, 0x4f7ffffe, v2
	v_cvt_u32_f32_e32 v2, v2
	v_mul_lo_u32 v5, v5, v2
	v_mul_hi_u32 v5, v2, v5
	v_add_u32_e32 v2, v2, v5
	s_waitcnt vmcnt(0)
	v_mul_hi_u32 v2, v4, v2
	v_mul_lo_u32 v5, v2, v3
	v_sub_u32_e32 v5, v4, v5
	v_add_u32_e32 v6, 1, v2
	v_cmp_ge_u32_e32 vcc, v5, v3
	v_add_u32_e32 v4, 1, v4
	s_nop 0
	v_cndmask_b32_e32 v2, v2, v6, vcc
	v_sub_u32_e32 v6, v5, v3
	v_cndmask_b32_e32 v5, v5, v6, vcc
	v_add_u32_e32 v6, 1, v2
	v_cmp_ge_u32_e32 vcc, v5, v3
	s_nop 1
	v_cndmask_b32_e32 v2, v2, v6, vcc
	v_mul_lo_u32 v5, v3, v2
	v_add_u32_e32 v3, v5, v3
	v_cmp_ne_u32_e32 vcc, v4, v3
	s_and_saveexec_b64 s[4:5], vcc
	s_xor_b64 s[4:5], exec, s[4:5]
	s_cbranch_execz .LBB0_84
	s_waitcnt lgkmcnt(0)
	buffer_inv sc1
	v_mov_b32_e32 v1, 0x2000
	global_load_dword v1, v1, s[2:3] offset:1024 sc1
	s_add_u32 s14, s2, 0x2400
	s_addc_u32 s15, s3, 0
	s_waitcnt vmcnt(0)
	v_cmp_eq_u32_e32 vcc, v1, v2
	s_and_saveexec_b64 s[6:7], vcc
	s_cbranch_execz .LBB0_83
	s_add_u32 s8, s48, 0x4200
	s_addc_u32 s9, s49, 0
	s_mov_b32 s26, 1
	s_mov_b64 s[16:17], 0
	v_mov_b32_e32 v1, 0
	s_branch .LBB0_74

.LBB0_83:
	s_or_b64 exec, exec, s[6:7]
	s_waitcnt vmcnt(0)
	s_waitcnt vmcnt(0)
.LBB0_84:
	s_andn2_saveexec_b64 s[4:5], s[4:5]
	s_cbranch_execz .LBB0_102
	s_mov_b64 s[4:5], exec
	buffer_wbl2 sc1
	s_waitcnt lgkmcnt(0)
	s_waitcnt vmcnt(0)
	buffer_inv sc1
	v_mbcnt_lo_u32_b32 v2, s4, 0
	v_mbcnt_hi_u32_b32 v2, s5, v2
	v_cmp_eq_u32_e32 vcc, 0, v2
	s_and_saveexec_b64 s[6:7], vcc
	s_cbranch_execz .LBB0_87
	s_bcnt1_i32_b64 s4, s[4:5]
	v_mov_b32_e32 v3, 0x7000
	v_mov_b32_e32 v4, s4
	global_atomic_add v3, v3, v4, s[48:49] offset:1024 sc0

.LBB0_99:
	s_or_b64 exec, exec, s[4:5]
	s_and_saveexec_b64 s[4:5], s[8:9]
	s_cbranch_execz .LBB0_101
	v_mov_b32_e32 v1, 1
	global_atomic_add v[2:3], v1, off
	v_mov_b32_e32 v2, 0x6400
	global_atomic_add v2, v1, s[48:49]
	v_add_u32_e32 v2, 0x100, v2
	global_atomic_add v2, v1, s[48:49]
	v_add_u32_e32 v2, 0x100, v2
	global_atomic_add v2, v1, s[48:49]
	v_add_u32_e32 v2, 0x100, v2
	global_atomic_add v2, v1, s[48:49]
	v_add_u32_e32 v2, 0x100, v2
	global_atomic_add v2, v1, s[48:49]
	v_add_u32_e32 v2, 0x100, v2
	global_atomic_add v2, v1, s[48:49]
	v_add_u32_e32 v2, 0x100, v2
	global_atomic_add v2, v1, s[48:49]
	v_add_u32_e32 v2, 0x100, v2
	global_atomic_add v2, v1, s[48:49]
	v_add_u32_e32 v2, 0x100, v2
	global_atomic_add v2, v1, s[48:49]
	v_add_u32_e32 v2, 0x100, v2
	global_atomic_add v2, v1, s[48:49]
	v_add_u32_e32 v2, 0x100, v2
	global_atomic_add v2, v1, s[48:49]
	v_add_u32_e32 v2, 0x100, v2
	global_atomic_add v2, v1, s[48:49]
	v_add_u32_e32 v2, 0x100, v2
	global_atomic_add v2, v1, s[48:49]
	v_add_u32_e32 v2, 0x100, v2
	global_atomic_add v2, v1, s[48:49]
	v_add_u32_e32 v2, 0x100, v2
	global_atomic_add v2, v1, s[48:49]
	v_add_u32_e32 v2, 0x100, v2
	global_atomic_add v2, v1, s[48:49]
.LBB0_101:
	s_or_b64 exec, exec, s[4:5]
	v_mov_b32_e32 v1, 0x2000
	v_mov_b32_e32 v2, 1
	s_waitcnt vmcnt(0)
	s_waitcnt vmcnt(0)

.LBB0_575:
	v_readlane_b32 s2, v253, 36
	s_lshl_b32 s2, s2, 8
	v_readlane_b32 s4, v253, 34
	v_readlane_b32 s5, v253, 35
	s_add_u32 s2, s4, s2
	s_addc_u32 s3, s5, 0
	v_mov_b32_e32 v2, 0x1000
	v_mov_b32_e32 v4, 1
	global_atomic_add v4, v2, v4, s[2:3] offset:1024 sc0
	v_cvt_f32_u32_e32 v2, v3
	v_sub_u32_e32 v5, 0, v3
	v_rcp_iflag_f32_e32 v2, v2
	s_nop 0
	v_mul_f32_e32 v2, 0x4f7ffffe, v2
	v_cvt_u32_f32_e32 v2, v2
	v_mul_lo_u32 v5, v5, v2
	v_mul_hi_u32 v5, v2, v5
	v_add_u32_e32 v2, v2, v5
	s_waitcnt vmcnt(0)
	v_mul_hi_u32 v2, v4, v2
	v_mul_lo_u32 v5, v2, v3
	v_sub_u32_e32 v5, v4, v5
	v_add_u32_e32 v6, 1, v2
	v_cmp_ge_u32_e32 vcc, v5, v3
	v_add_u32_e32 v4, 1, v4
	s_nop 0
	v_cndmask_b32_e32 v2, v2, v6, vcc
	v_sub_u32_e32 v6, v5, v3
	v_cndmask_b32_e32 v5, v5, v6, vcc
	v_add_u32_e32 v6, 1, v2
	v_cmp_ge_u32_e32 vcc, v5, v3
	s_nop 1
	v_cndmask_b32_e32 v2, v2, v6, vcc
	v_mul_lo_u32 v5, v3, v2
	v_add_u32_e32 v3, v5, v3
	v_cmp_ne_u32_e32 vcc, v4, v3
	s_and_saveexec_b64 s[4:5], vcc
	s_xor_b64 s[4:5], exec, s[4:5]
	s_cbranch_execz .LBB0_589
	s_waitcnt lgkmcnt(0)
	buffer_inv sc1
	v_mov_b32_e32 v1, 0x2000
	global_load_dword v1, v1, s[2:3] offset:1024 sc1
	s_add_u32 s10, s2, 0x2400
	s_addc_u32 s11, s3, 0
	s_waitcnt vmcnt(0)
	v_cmp_eq_u32_e32 vcc, v1, v2
	s_and_saveexec_b64 s[6:7], vcc
	s_cbranch_execz .LBB0_588
	s_add_u32 s8, s48, 0x4200
	s_addc_u32 s9, s49, 0
	s_mov_b32 s22, 1
	s_mov_b64 s[12:13], 0
	v_mov_b32_e32 v1, 0
	s_branch .LBB0_579

.LBB0_959:
	v_readlane_b32 s4, v253, 36
	s_lshl_b32 s4, s4, 8
	v_readlane_b32 s6, v253, 34
	v_readlane_b32 s7, v253, 35
	s_add_u32 s4, s6, s4
	s_addc_u32 s5, s7, 0
	v_mov_b32_e32 v2, 0x1000
	v_mov_b32_e32 v4, 1
	global_atomic_add v4, v2, v4, s[4:5] offset:1024 sc0
	v_cvt_f32_u32_e32 v2, v3
	v_sub_u32_e32 v5, 0, v3
	v_rcp_iflag_f32_e32 v2, v2
	s_nop 0
	v_mul_f32_e32 v2, 0x4f7ffffe, v2
	v_cvt_u32_f32_e32 v2, v2
	v_mul_lo_u32 v5, v5, v2
	v_mul_hi_u32 v5, v2, v5
	v_add_u32_e32 v2, v2, v5
	s_waitcnt vmcnt(0)
	v_mul_hi_u32 v2, v4, v2
	v_mul_lo_u32 v5, v2, v3
	v_sub_u32_e32 v5, v4, v5
	v_add_u32_e32 v6, 1, v2
	v_cmp_ge_u32_e32 vcc, v5, v3
	v_add_u32_e32 v4, 1, v4
	s_nop 0
	v_cndmask_b32_e32 v2, v2, v6, vcc
	v_sub_u32_e32 v6, v5, v3
	v_cndmask_b32_e32 v5, v5, v6, vcc
	v_add_u32_e32 v6, 1, v2
	v_cmp_ge_u32_e32 vcc, v5, v3
	s_nop 1
	v_cndmask_b32_e32 v2, v2, v6, vcc
	v_mul_lo_u32 v5, v3, v2
	v_add_u32_e32 v3, v5, v3
	v_cmp_ne_u32_e32 vcc, v4, v3
	s_and_saveexec_b64 s[6:7], vcc
	s_xor_b64 s[6:7], exec, s[6:7]
	s_cbranch_execz .LBB0_973
	s_waitcnt lgkmcnt(0)
	buffer_inv sc1
	v_mov_b32_e32 v1, 0x2000
	global_load_dword v1, v1, s[4:5] offset:1024 sc1
	s_add_u32 s12, s4, 0x2400
	s_addc_u32 s13, s5, 0
	s_waitcnt vmcnt(0)
	v_cmp_eq_u32_e32 vcc, v1, v2
	s_and_saveexec_b64 s[8:9], vcc
	s_cbranch_execz .LBB0_972
	s_add_u32 s10, s48, 0x4200
	s_addc_u32 s11, s49, 0
	s_mov_b32 s24, 1
	s_mov_b64 s[14:15], 0
	v_mov_b32_e32 v1, 0
	s_branch .LBB0_963

.LBB0_972:
	s_or_b64 exec, exec, s[8:9]
	s_waitcnt vmcnt(0)
	s_waitcnt vmcnt(0)
.LBB0_973:
	s_andn2_saveexec_b64 s[6:7], s[6:7]
	s_cbranch_execz .LBB0_991
	s_mov_b64 s[6:7], exec
	buffer_wbl2 sc1
	s_waitcnt lgkmcnt(0)
	s_waitcnt vmcnt(0)
	buffer_inv sc1
	v_mbcnt_lo_u32_b32 v2, s6, 0
	v_mbcnt_hi_u32_b32 v2, s7, v2
	v_cmp_eq_u32_e32 vcc, 0, v2
	s_and_saveexec_b64 s[8:9], vcc
	s_cbranch_execz .LBB0_976
	s_bcnt1_i32_b64 s6, s[6:7]
	v_mov_b32_e32 v3, 0x7000
	v_mov_b32_e32 v4, s6
	global_atomic_add v3, v3, v4, s[48:49] offset:1024 sc0

.LBB0_988:
	s_or_b64 exec, exec, s[6:7]
	s_and_saveexec_b64 s[6:7], s[10:11]
	s_cbranch_execz .LBB0_990
	v_mov_b32_e32 v1, 1
	global_atomic_add v[2:3], v1, off
	v_mov_b32_e32 v2, 0x6400
	global_atomic_add v2, v1, s[48:49]
	v_add_u32_e32 v2, 0x100, v2
	global_atomic_add v2, v1, s[48:49]
	v_add_u32_e32 v2, 0x100, v2
	global_atomic_add v2, v1, s[48:49]
	v_add_u32_e32 v2, 0x100, v2
	global_atomic_add v2, v1, s[48:49]
	v_add_u32_e32 v2, 0x100, v2
	global_atomic_add v2, v1, s[48:49]
	v_add_u32_e32 v2, 0x100, v2
	global_atomic_add v2, v1, s[48:49]
	v_add_u32_e32 v2, 0x100, v2
	global_atomic_add v2, v1, s[48:49]
	v_add_u32_e32 v2, 0x100, v2
	global_atomic_add v2, v1, s[48:49]
	v_add_u32_e32 v2, 0x100, v2
	global_atomic_add v2, v1, s[48:49]
	v_add_u32_e32 v2, 0x100, v2
	global_atomic_add v2, v1, s[48:49]
	v_add_u32_e32 v2, 0x100, v2
	global_atomic_add v2, v1, s[48:49]
	v_add_u32_e32 v2, 0x100, v2
	global_atomic_add v2, v1, s[48:49]
	v_add_u32_e32 v2, 0x100, v2
	global_atomic_add v2, v1, s[48:49]
	v_add_u32_e32 v2, 0x100, v2
	global_atomic_add v2, v1, s[48:49]
	v_add_u32_e32 v2, 0x100, v2
	global_atomic_add v2, v1, s[48:49]
	v_add_u32_e32 v2, 0x100, v2
	global_atomic_add v2, v1, s[48:49]
.LBB0_990:
	s_or_b64 exec, exec, s[6:7]
	v_mov_b32_e32 v1, 0x2000
	v_mov_b32_e32 v2, 1
	s_waitcnt vmcnt(0)
	s_waitcnt vmcnt(0)

.LBB0_1572:
	v_readlane_b32 s2, v253, 36
	s_lshl_b32 s2, s2, 8
	v_readlane_b32 s4, v253, 34
	v_readlane_b32 s5, v253, 35
	s_add_u32 s2, s4, s2
	s_addc_u32 s3, s5, 0
	v_mov_b32_e32 v3, 0x1000
	v_mov_b32_e32 v5, 1
	global_atomic_add v5, v3, v5, s[2:3] offset:1024 sc0
	v_cvt_f32_u32_e32 v3, v4
	v_sub_u32_e32 v6, 0, v4
	v_rcp_iflag_f32_e32 v3, v3
	s_nop 0
	v_mul_f32_e32 v3, 0x4f7ffffe, v3
	v_cvt_u32_f32_e32 v3, v3
	v_mul_lo_u32 v6, v6, v3
	v_mul_hi_u32 v6, v3, v6
	v_add_u32_e32 v3, v3, v6
	s_waitcnt vmcnt(0)
	v_mul_hi_u32 v3, v5, v3
	v_mul_lo_u32 v6, v3, v4
	v_sub_u32_e32 v6, v5, v6
	v_add_u32_e32 v7, 1, v3
	v_cmp_ge_u32_e32 vcc, v6, v4
	v_add_u32_e32 v5, 1, v5
	s_nop 0
	v_cndmask_b32_e32 v3, v3, v7, vcc
	v_sub_u32_e32 v7, v6, v4
	v_cndmask_b32_e32 v6, v6, v7, vcc
	v_add_u32_e32 v7, 1, v3
	v_cmp_ge_u32_e32 vcc, v6, v4
	s_nop 1
	v_cndmask_b32_e32 v3, v3, v7, vcc
	v_mul_lo_u32 v6, v4, v3
	v_add_u32_e32 v4, v6, v4
	v_cmp_ne_u32_e32 vcc, v5, v4
	s_and_saveexec_b64 s[4:5], vcc
	s_xor_b64 s[4:5], exec, s[4:5]
	s_cbranch_execz .LBB0_1586
	s_waitcnt lgkmcnt(0)
	buffer_inv sc1
	v_mov_b32_e32 v2, 0x2000
	global_load_dword v2, v2, s[2:3] offset:1024 sc1
	s_add_u32 s10, s2, 0x2400
	s_addc_u32 s11, s3, 0
	s_waitcnt vmcnt(0)
	v_cmp_eq_u32_e32 vcc, v2, v3
	s_and_saveexec_b64 s[6:7], vcc
	s_cbranch_execz .LBB0_1585
	s_add_u32 s8, s48, 0x4200
	s_addc_u32 s9, s49, 0
	s_mov_b32 s22, 1
	s_mov_b64 s[12:13], 0
	v_mov_b32_e32 v2, 0
	s_branch .LBB0_1576

.LBB0_1586:
	s_andn2_saveexec_b64 s[4:5], s[4:5]
	s_cbranch_execz .LBB0_1604
	s_mov_b64 s[4:5], exec
	buffer_wbl2 sc1
	s_waitcnt lgkmcnt(0)
	s_waitcnt vmcnt(0)
	buffer_inv sc1
	v_mbcnt_lo_u32_b32 v3, s4, 0
	v_mbcnt_hi_u32_b32 v3, s5, v3
	v_cmp_eq_u32_e32 vcc, 0, v3
	s_and_saveexec_b64 s[6:7], vcc
	s_cbranch_execz .LBB0_1589
	s_bcnt1_i32_b64 s4, s[4:5]
	v_mov_b32_e32 v4, 0x7000
	v_mov_b32_e32 v5, s4
	global_atomic_add v4, v4, v5, s[48:49] offset:1024 sc0

.LBB0_1601:
	s_or_b64 exec, exec, s[4:5]
	s_and_saveexec_b64 s[4:5], s[8:9]
	s_cbranch_execz .LBB0_1603
	v_mov_b32_e32 v4, 1
	global_atomic_add v[2:3], v4, off
	v_mov_b32_e32 v2, 0x6400
	global_atomic_add v2, v4, s[48:49]
	v_add_u32_e32 v2, 0x100, v2
	global_atomic_add v2, v4, s[48:49]
	v_add_u32_e32 v2, 0x100, v2
	global_atomic_add v2, v4, s[48:49]
	v_add_u32_e32 v2, 0x100, v2
	global_atomic_add v2, v4, s[48:49]
	v_add_u32_e32 v2, 0x100, v2
	global_atomic_add v2, v4, s[48:49]
	v_add_u32_e32 v2, 0x100, v2
	global_atomic_add v2, v4, s[48:49]
	v_add_u32_e32 v2, 0x100, v2
	global_atomic_add v2, v4, s[48:49]
	v_add_u32_e32 v2, 0x100, v2
	global_atomic_add v2, v4, s[48:49]
	v_add_u32_e32 v2, 0x100, v2
	global_atomic_add v2, v4, s[48:49]
	v_add_u32_e32 v2, 0x100, v2
	global_atomic_add v2, v4, s[48:49]
	v_add_u32_e32 v2, 0x100, v2
	global_atomic_add v2, v4, s[48:49]
	v_add_u32_e32 v2, 0x100, v2
	global_atomic_add v2, v4, s[48:49]
	v_add_u32_e32 v2, 0x100, v2
	global_atomic_add v2, v4, s[48:49]
	v_add_u32_e32 v2, 0x100, v2
	global_atomic_add v2, v4, s[48:49]
	v_add_u32_e32 v2, 0x100, v2
	global_atomic_add v2, v4, s[48:49]
	v_add_u32_e32 v2, 0x100, v2
	global_atomic_add v2, v4, s[48:49]
.LBB0_1603:
	s_or_b64 exec, exec, s[4:5]
	v_mov_b32_e32 v2, 0x2000
	v_mov_b32_e32 v3, 1
	s_waitcnt vmcnt(0)
	s_waitcnt vmcnt(0)

.LBB0_1790:
	v_readlane_b32 s4, v253, 36
	s_lshl_b32 s4, s4, 8
	v_readlane_b32 s6, v253, 34
	v_readlane_b32 s7, v253, 35
	s_add_u32 s4, s6, s4
	s_addc_u32 s5, s7, 0
	v_mov_b32_e32 v3, 0x1000
	v_mov_b32_e32 v5, 1
	global_atomic_add v5, v3, v5, s[4:5] offset:1024 sc0
	v_cvt_f32_u32_e32 v3, v4
	v_sub_u32_e32 v6, 0, v4
	v_rcp_iflag_f32_e32 v3, v3
	s_nop 0
	v_mul_f32_e32 v3, 0x4f7ffffe, v3
	v_cvt_u32_f32_e32 v3, v3
	v_mul_lo_u32 v6, v6, v3
	v_mul_hi_u32 v6, v3, v6
	v_add_u32_e32 v3, v3, v6
	s_waitcnt vmcnt(0)
	v_mul_hi_u32 v3, v5, v3
	v_mul_lo_u32 v6, v3, v4
	v_sub_u32_e32 v6, v5, v6
	v_add_u32_e32 v7, 1, v3
	v_cmp_ge_u32_e32 vcc, v6, v4
	v_add_u32_e32 v5, 1, v5
	s_nop 0
	v_cndmask_b32_e32 v3, v3, v7, vcc
	v_sub_u32_e32 v7, v6, v4
	v_cndmask_b32_e32 v6, v6, v7, vcc
	v_add_u32_e32 v7, 1, v3
	v_cmp_ge_u32_e32 vcc, v6, v4
	s_nop 1
	v_cndmask_b32_e32 v3, v3, v7, vcc
	v_mul_lo_u32 v6, v4, v3
	v_add_u32_e32 v4, v6, v4
	v_cmp_ne_u32_e32 vcc, v5, v4
	s_and_saveexec_b64 s[6:7], vcc
	s_xor_b64 s[6:7], exec, s[6:7]
	s_cbranch_execz .LBB0_1804
	s_waitcnt lgkmcnt(0)
	buffer_inv sc1
	v_mov_b32_e32 v2, 0x2000
	global_load_dword v2, v2, s[4:5] offset:1024 sc1
	s_add_u32 s14, s4, 0x2400
	s_addc_u32 s15, s5, 0
	s_waitcnt vmcnt(0)
	v_cmp_eq_u32_e32 vcc, v2, v3
	s_and_saveexec_b64 s[10:11], vcc
	s_cbranch_execz .LBB0_1803
	s_add_u32 s12, s48, 0x4200
	s_addc_u32 s13, s49, 0
	s_mov_b32 s26, 1
	s_mov_b64 s[16:17], 0
	v_mov_b32_e32 v2, 0
	s_branch .LBB0_1794

.LBB0_1803:
	s_or_b64 exec, exec, s[10:11]
	s_waitcnt vmcnt(0)
	s_waitcnt vmcnt(0)
.LBB0_1804:
	s_andn2_saveexec_b64 s[6:7], s[6:7]
	s_cbranch_execz .LBB0_1822
	s_mov_b64 s[6:7], exec
	buffer_wbl2 sc1
	s_waitcnt lgkmcnt(0)
	s_waitcnt vmcnt(0)
	buffer_inv sc1
	v_mbcnt_lo_u32_b32 v3, s6, 0
	v_mbcnt_hi_u32_b32 v3, s7, v3
	v_cmp_eq_u32_e32 vcc, 0, v3
	s_and_saveexec_b64 s[10:11], vcc
	s_cbranch_execz .LBB0_1807
	s_bcnt1_i32_b64 s6, s[6:7]
	v_mov_b32_e32 v4, 0x7000
	v_mov_b32_e32 v5, s6
	global_atomic_add v4, v4, v5, s[48:49] offset:1024 sc0

.LBB0_1819:
	s_or_b64 exec, exec, s[6:7]
	s_and_saveexec_b64 s[6:7], s[12:13]
	s_cbranch_execz .LBB0_1821
	v_mov_b32_e32 v4, 1
	global_atomic_add v[2:3], v4, off
	v_mov_b32_e32 v2, 0x6400
	global_atomic_add v2, v4, s[48:49]
	v_add_u32_e32 v2, 0x100, v2
	global_atomic_add v2, v4, s[48:49]
	v_add_u32_e32 v2, 0x100, v2
	global_atomic_add v2, v4, s[48:49]
	v_add_u32_e32 v2, 0x100, v2
	global_atomic_add v2, v4, s[48:49]
	v_add_u32_e32 v2, 0x100, v2
	global_atomic_add v2, v4, s[48:49]
	v_add_u32_e32 v2, 0x100, v2
	global_atomic_add v2, v4, s[48:49]
	v_add_u32_e32 v2, 0x100, v2
	global_atomic_add v2, v4, s[48:49]
	v_add_u32_e32 v2, 0x100, v2
	global_atomic_add v2, v4, s[48:49]
	v_add_u32_e32 v2, 0x100, v2
	global_atomic_add v2, v4, s[48:49]
	v_add_u32_e32 v2, 0x100, v2
	global_atomic_add v2, v4, s[48:49]
	v_add_u32_e32 v2, 0x100, v2
	global_atomic_add v2, v4, s[48:49]
	v_add_u32_e32 v2, 0x100, v2
	global_atomic_add v2, v4, s[48:49]
	v_add_u32_e32 v2, 0x100, v2
	global_atomic_add v2, v4, s[48:49]
	v_add_u32_e32 v2, 0x100, v2
	global_atomic_add v2, v4, s[48:49]
	v_add_u32_e32 v2, 0x100, v2
	global_atomic_add v2, v4, s[48:49]
	v_add_u32_e32 v2, 0x100, v2
	global_atomic_add v2, v4, s[48:49]
.LBB0_1821:
	s_or_b64 exec, exec, s[6:7]
	v_mov_b32_e32 v2, 0x2000
	v_mov_b32_e32 v3, 1
	s_waitcnt vmcnt(0)
	s_waitcnt vmcnt(0)

.LBB0_1876:
	v_readlane_b32 s4, v253, 36
	s_lshl_b32 s4, s4, 8
	v_readlane_b32 s6, v253, 34
	v_readlane_b32 s7, v253, 35
	s_add_u32 s4, s6, s4
	s_addc_u32 s5, s7, 0
	v_mov_b32_e32 v3, 0x1000
	v_mov_b32_e32 v5, 1
	global_atomic_add v5, v3, v5, s[4:5] offset:1024 sc0
	v_cvt_f32_u32_e32 v3, v4
	v_sub_u32_e32 v6, 0, v4
	v_rcp_iflag_f32_e32 v3, v3
	s_nop 0
	v_mul_f32_e32 v3, 0x4f7ffffe, v3
	v_cvt_u32_f32_e32 v3, v3
	v_mul_lo_u32 v6, v6, v3
	v_mul_hi_u32 v6, v3, v6
	v_add_u32_e32 v3, v3, v6
	s_waitcnt vmcnt(0)
	v_mul_hi_u32 v3, v5, v3
	v_mul_lo_u32 v6, v3, v4
	v_sub_u32_e32 v6, v5, v6
	v_add_u32_e32 v7, 1, v3
	v_cmp_ge_u32_e32 vcc, v6, v4
	v_add_u32_e32 v5, 1, v5
	s_nop 0
	v_cndmask_b32_e32 v3, v3, v7, vcc
	v_sub_u32_e32 v7, v6, v4
	v_cndmask_b32_e32 v6, v6, v7, vcc
	v_add_u32_e32 v7, 1, v3
	v_cmp_ge_u32_e32 vcc, v6, v4
	s_nop 1
	v_cndmask_b32_e32 v3, v3, v7, vcc
	v_mul_lo_u32 v6, v4, v3
	v_add_u32_e32 v4, v6, v4
	v_cmp_ne_u32_e32 vcc, v5, v4
	s_and_saveexec_b64 s[6:7], vcc
	s_xor_b64 s[6:7], exec, s[6:7]
	s_cbranch_execz .LBB0_1890
	s_waitcnt lgkmcnt(0)
	buffer_inv sc1
	v_mov_b32_e32 v2, 0x2000
	global_load_dword v2, v2, s[4:5] offset:1024 sc1
	s_add_u32 s12, s4, 0x2400
	s_addc_u32 s13, s5, 0
	s_waitcnt vmcnt(0)
	v_cmp_eq_u32_e32 vcc, v2, v3
	s_and_saveexec_b64 s[8:9], vcc
	s_cbranch_execz .LBB0_1889
	s_add_u32 s10, s48, 0x4200
	s_addc_u32 s11, s49, 0
	s_mov_b32 s24, 1
	s_mov_b64 s[14:15], 0
	v_mov_b32_e32 v2, 0
	s_branch .LBB0_1880

.LBB0_1890:
	s_andn2_saveexec_b64 s[6:7], s[6:7]
	s_cbranch_execz .LBB0_1908
	s_mov_b64 s[6:7], exec
	buffer_wbl2 sc1
	s_waitcnt lgkmcnt(0)
	s_waitcnt vmcnt(0)
	buffer_inv sc1
	v_mbcnt_lo_u32_b32 v3, s6, 0
	v_mbcnt_hi_u32_b32 v3, s7, v3
	v_cmp_eq_u32_e32 vcc, 0, v3
	s_and_saveexec_b64 s[8:9], vcc
	s_cbranch_execz .LBB0_1893
	s_bcnt1_i32_b64 s6, s[6:7]
	v_mov_b32_e32 v4, 0x7000
	v_mov_b32_e32 v5, s6
	global_atomic_add v4, v4, v5, s[48:49] offset:1024 sc0

.LBB0_1905:
	s_or_b64 exec, exec, s[6:7]
	s_and_saveexec_b64 s[6:7], s[10:11]
	s_cbranch_execz .LBB0_1907
	v_mov_b32_e32 v4, 1
	global_atomic_add v[2:3], v4, off
	v_mov_b32_e32 v2, 0x6400
	global_atomic_add v2, v4, s[48:49]
	v_add_u32_e32 v2, 0x100, v2
	global_atomic_add v2, v4, s[48:49]
	v_add_u32_e32 v2, 0x100, v2
	global_atomic_add v2, v4, s[48:49]
	v_add_u32_e32 v2, 0x100, v2
	global_atomic_add v2, v4, s[48:49]
	v_add_u32_e32 v2, 0x100, v2
	global_atomic_add v2, v4, s[48:49]
	v_add_u32_e32 v2, 0x100, v2
	global_atomic_add v2, v4, s[48:49]
	v_add_u32_e32 v2, 0x100, v2
	global_atomic_add v2, v4, s[48:49]
	v_add_u32_e32 v2, 0x100, v2
	global_atomic_add v2, v4, s[48:49]
	v_add_u32_e32 v2, 0x100, v2
	global_atomic_add v2, v4, s[48:49]
	v_add_u32_e32 v2, 0x100, v2
	global_atomic_add v2, v4, s[48:49]
	v_add_u32_e32 v2, 0x100, v2
	global_atomic_add v2, v4, s[48:49]
	v_add_u32_e32 v2, 0x100, v2
	global_atomic_add v2, v4, s[48:49]
	v_add_u32_e32 v2, 0x100, v2
	global_atomic_add v2, v4, s[48:49]
	v_add_u32_e32 v2, 0x100, v2
	global_atomic_add v2, v4, s[48:49]
	v_add_u32_e32 v2, 0x100, v2
	global_atomic_add v2, v4, s[48:49]
	v_add_u32_e32 v2, 0x100, v2
	global_atomic_add v2, v4, s[48:49]
